# a5 + exp2 tile experts via v_readlane (no per-unit load) + exp1 gathered-row tables in LDS and tile experts via v_readlane (no global load/vmcnt wait between epilogue and K loop)
# speedup vs baseline: 1.0153x; 1.0060x over previous
.LBB0_3468:
	s_lshl_b32 s2, s4, 7
	s_mov_b32 s3, s40
	s_lshl_b64 s[2:3], s[2:3], 2
	s_add_u32 s2, s46, s2
	s_addc_u32 s3, s47, s3
	global_load_dword v2, v1, s[2:3] offset:260
	v_readlane_b32 s2, v254, 60
	v_readlane_b32 s3, v254, 61
	s_mul_i32 s42, s4, 0x28000
	s_andn2_b64 vcc, exec, s[2:3]
	v_writelane_b32 v254, s4, 56
	s_mul_i32 s2, s4, 0x280
	s_waitcnt vmcnt(0)
	v_readfirstlane_b32 s81, v2
	s_cbranch_vccnz .LBB0_3496
	s_mov_b32 s43, s40
	s_lshl_b64 s[4:5], s[42:43], 2
	v_readlane_b32 s8, v255, 6
	v_readlane_b32 s9, v255, 7
	s_add_u32 s8, s8, s4
	s_mov_b32 s3, s40
	s_addc_u32 s9, s9, s5
	s_lshl_b64 s[4:5], s[2:3], 2
	v_readlane_b32 s10, v254, 58
	v_readlane_b32 s11, v254, 59
	s_add_u32 s3, s10, s4
	s_addc_u32 s28, s11, s5
	s_lshl_b32 s29, s81, 2
	s_cmp_lt_i32 s92, s29
	s_cselect_b64 s[10:11], -1, 0
	s_cmp_lt_i32 s37, s81
	s_mov_b32 s30, 0
	s_cselect_b64 s[90:91], -1, 0
	v_mov_b32_e32 v241, s92
	v_and_b32_e32 v246, 7, v241
	v_bfe_u32 v241, v241, 3, 3
	v_lshl_add_u32 v241, v246, 3, v241
	v_mbcnt_lo_u32_b32 v242, -1, 0
	v_mbcnt_hi_u32_b32 v242, -1, v242
	v_lshl_add_u32 v242, v242, 6, v241
	v_lshlrev_b32_e32 v242, 2, v242
	v_mov_b32_e32 v243, 0
	v_mov_b32_e32 v246, s3
	v_mov_b32_e32 v247, s28
	v_lshl_add_u64 v[246:247], v[242:243], 0, v[246:247]
	global_load_dword v242, v[246:247], off
	v_and_b32_e32 v238, 0xff, v0
	v_lshrrev_b32_e32 v239, 8, v0
	v_lshl_add_u32 v240, v239, 6, v241
	v_lshl_add_u32 v240, v240, 8, v238
	v_lshlrev_b32_e32 v240, 2, v240
	global_load_dword v244, v240, s[8:9]
	v_add_u32_e32 v240, 0x20000, v240
	global_load_dword v245, v240, s[8:9]
	v_add_u32_e32 v240, 0x20000, v240
	global_load_dword v248, v240, s[8:9]
	v_add_u32_e32 v240, 0x20000, v240
	global_load_dword v249, v240, s[8:9]
	v_add_u32_e32 v240, 0x20000, v240
	global_load_dword v250, v240, s[8:9]
	v_lshlrev_b32_e32 v238, 2, v238
	v_lshl_add_u32 v238, v239, 10, v238
	v_add_u32_e32 v238, 0x20000, v238
	s_waitcnt vmcnt(0)
	ds_write_b32 v238, v244
	ds_write_b32 v238, v245 offset:2048
	ds_write_b32 v238, v248 offset:4096
	ds_write_b32 v238, v249 offset:6144
	ds_write_b32 v238, v250 offset:8192
	s_waitcnt lgkmcnt(0)
	s_barrier
	s_branch .LBB0_3472

.LBB0_3485:
	s_lshr_b32 s17, s16, 6
	s_mov_b64 s[24:25], -1
	s_mov_b32 s51, s15
	s_mov_b32 s87, s16
	s_nop 3
	v_readlane_b32 s14, v242, s17
.LBB0_3486:
	s_xor_b64 s[16:17], s[24:25], -1
	s_and_b64 vcc, exec, s[16:17]
	v_mov_b32_e32 v194, v168
	v_mov_b32_e32 v195, v170
	v_mov_b32_e32 v196, v172
	v_mov_b32_e32 v197, v174
	s_cbranch_vccnz .LBB0_3488
	s_lshr_b32 s15, s87, 6
	s_lshl_b32 s15, s15, 10
	s_add_i32 s15, s15, 0x20000
	v_lshl_add_u32 v194, v188, 2, s15
	v_lshl_add_u32 v195, v190, 2, s15
	ds_read_b32 v196, v194 offset:512
	ds_read_b32 v197, v195 offset:512
	ds_read_b32 v194, v194
	ds_read_b32 v195, v195
	s_waitcnt lgkmcnt(0)
	v_lshl_add_u32 v194, v194, 11, v189
	v_lshl_add_u32 v195, v195, 11, v191
	v_lshl_add_u32 v196, v196, 11, v189
	v_lshl_add_u32 v197, v197, 11, v191
	s_nop 0

.LBB0_3603:
	v_readlane_b32 s0, v255, 0
	v_readlane_b32 s1, v255, 1
	s_andn2_b64 vcc, exec, s[0:1]
	s_cbranch_vccnz .LBB0_3649
	s_mov_b32 s3, s40
	s_lshl_b64 s[0:1], s[2:3], 2
	v_readlane_b32 s2, v254, 58
	v_readlane_b32 s3, v254, 59
	s_add_u32 s33, s2, s0
	s_mov_b32 s43, s40
	s_addc_u32 s36, s3, s1
	s_lshl_b64 s[0:1], s[42:43], 3
	v_readlane_b32 s2, v255, 4
	v_readlane_b32 s3, v255, 5
	s_add_u32 s0, s2, s0
	s_addc_u32 s1, s3, s1
	s_lshl_b32 s4, s81, 3
	s_cmp_lt_i32 s92, s4
	s_cselect_b64 s[2:3], -1, 0
	v_writelane_b32 v254, s2, 42
	s_nop 1
	v_writelane_b32 v254, s3, 43
	s_mov_b32 s2, 0
	v_readlane_b32 s3, v254, 40
	s_cmp_lt_i32 s3, s81
	s_cselect_b64 s[8:9], -1, 0
	v_writelane_b32 v254, s8, 44
	s_nop 1
	v_writelane_b32 v254, s9, 45
	v_mbcnt_lo_u32_b32 v242, -1, 0
	v_mbcnt_hi_u32_b32 v242, -1, v242
	s_and_b32 s8, s92, 7
	s_lshl_b32 s8, s8, 2
	s_bfe_u32 s9, s92, 0x20003
	s_add_i32 s8, s8, s9
	v_lshl_add_u32 v242, v242, 5, s8
	v_lshlrev_b32_e32 v242, 2, v242
	s_mov_b32 s8, s33
	s_mov_b32 s9, s36
	s_nop 0
	global_load_dword v242, v242, s[8:9]
	s_waitcnt vmcnt(0)
	s_nop 0
	s_nop 0
	s_nop 0
	s_nop 0
	s_nop 0
	s_nop 0
	s_nop 0
	s_nop 0
	s_nop 0
	s_nop 0
	s_nop 0
	s_nop 0
	s_nop 0
	s_nop 0
	s_branch .LBB0_3607

.LBB0_3624:
	s_lshr_b32 s27, s26, 5
	s_mov_b64 s[16:17], -1
	s_mov_b32 s60, s13
	s_mov_b32 s22, s26
	s_nop 3
	s_nop 0
	s_nop 0
	s_nop 0
	s_nop 0
	v_readlane_b32 s24, v242, s27
